# P10: non-first units skip accumulator zeroing (first-touch MFMA takes C=0 in a peeled first K-iteration), relaxed vmcnt there, drop 6x s_nop 15 before the epilogue
# speedup vs baseline: 1.1223x; 1.0095x over previous
.LBB0_1421:
	s_mov_b32 s98, 0
	s_cmp_lt_i32 s60, 11
	s_cselect_b64 s[8:9], -1, 0
	s_and_b64 s[0:1], s[8:9], s[0:1]
	s_andn2_b64 vcc, exec, s[0:1]
	s_cbranch_vccnz .LBB0_1450
	v_readlane_b32 s0, v252, 2
	v_readlane_b32 s2, v252, 4
	v_readlane_b32 s3, v252, 5
	s_add_u32 s4, s2, 0x24300000
	s_addc_u32 s2, s3, 0
	s_cmpk_gt_u32 s63, 0x7f
	v_readlane_b32 s1, v252, 3
	s_waitcnt vmcnt(0) lgkmcnt(0)
	s_barrier
	s_cbranch_scc1 .LBB0_1426
	s_mul_i32 s0, s97, 0x108
	s_add_i32 s3, s0, 0
	s_and_b32 s0, s63, 64
	v_readlane_b32 s12, v252, 2
	s_add_i32 s3, s3, 0x24000
	s_lshl_b32 s0, s0, 2
	v_readlane_b32 s14, v252, 4
	v_readlane_b32 s15, v252, 5
	s_add_u32 s0, s14, s0
	v_lshlrev_b32_e32 v2, 2, v206
	s_addc_u32 s1, s15, 0
	v_mov_b32_e32 v3, 0
	v_lshl_add_u64 v[4:5], s[0:1], 0, v[2:3]
	v_add_co_u32_e32 v4, vcc, 0x10000, v4
	v_mbcnt_lo_u32_b32 v3, -1, 0
	s_nop 0
	v_addc_co_u32_e32 v5, vcc, 0, v5, vcc
	global_load_dword v1, v[4:5], off sc1
	v_mbcnt_hi_u32_b32 v3, -1, v3
	v_and_b32_e32 v4, 64, v3
	v_add_u32_e32 v5, -1, v3
	v_cmp_lt_i32_e32 vcc, v5, v4
	v_add_u32_e32 v6, -2, v3
	v_add_u32_e32 v7, -4, v3
	v_cndmask_b32_e32 v5, v5, v3, vcc
	v_lshlrev_b32_e32 v5, 2, v5
	v_cmp_lt_i32_e32 vcc, v6, v4
	v_add_u32_e32 v8, -8, v3
	v_add_u32_e32 v9, -16, v3
	v_cndmask_b32_e32 v6, v6, v3, vcc
	v_cmp_ne_u32_e32 vcc, 0, v206
	v_lshlrev_b32_e32 v6, 2, v6
	v_cmp_lt_u32_e64 s[0:1], 31, v206
	v_readlane_b32 s13, v252, 3
	s_waitcnt vmcnt(0)
	v_add_u32_e32 v1, 0xff, v1
	v_and_b32_e32 v1, 0xffffff00, v1
	ds_bpermute_b32 v5, v5, v1
	s_waitcnt lgkmcnt(0)
	v_cndmask_b32_e32 v5, 0, v5, vcc
	v_add_u32_e32 v5, v5, v1
	ds_bpermute_b32 v6, v6, v5
	v_cmp_lt_i32_e32 vcc, v7, v4
	s_nop 1
	v_cndmask_b32_e32 v7, v7, v3, vcc
	v_cmp_lt_u32_e32 vcc, 1, v206
	v_lshlrev_b32_e32 v7, 2, v7
	s_waitcnt lgkmcnt(0)
	v_cndmask_b32_e32 v6, 0, v6, vcc
	v_add_u32_e32 v5, v6, v5
	ds_bpermute_b32 v6, v7, v5
	v_cmp_lt_i32_e32 vcc, v8, v4
	s_nop 1
	v_cndmask_b32_e32 v7, v8, v3, vcc
	v_cmp_lt_u32_e32 vcc, 3, v206
	v_lshlrev_b32_e32 v7, 2, v7
	s_waitcnt lgkmcnt(0)
	v_cndmask_b32_e32 v6, 0, v6, vcc
	v_add_u32_e32 v5, v6, v5
	ds_bpermute_b32 v6, v7, v5
	v_cmp_lt_i32_e32 vcc, v9, v4
	s_nop 1
	v_cndmask_b32_e32 v7, v9, v3, vcc
	v_cmp_lt_u32_e32 vcc, 7, v206
	v_lshlrev_b32_e32 v7, 2, v7
	s_waitcnt lgkmcnt(0)
	v_cndmask_b32_e32 v6, 0, v6, vcc
	v_add_u32_e32 v5, v6, v5
	ds_bpermute_b32 v6, v7, v5
	v_subrev_u32_e32 v7, 32, v3
	v_cmp_lt_i32_e32 vcc, v7, v4
	s_nop 1
	v_cndmask_b32_e32 v3, v7, v3, vcc
	v_cmp_lt_u32_e32 vcc, 15, v206
	v_lshlrev_b32_e32 v3, 2, v3
	s_waitcnt lgkmcnt(0)
	v_cndmask_b32_e32 v4, 0, v6, vcc
	v_add_u32_e32 v4, v4, v5
	ds_bpermute_b32 v3, v3, v4
	v_add_u32_e32 v5, s3, v2
	v_cmp_eq_u32_e32 vcc, 63, v206
	s_waitcnt lgkmcnt(0)
	v_cndmask_b32_e64 v2, 0, v3, s[0:1]
	v_add_u32_e32 v2, v2, v4
	v_sub_u32_e32 v1, v2, v1
	ds_write_b32 v5, v1
	s_and_saveexec_b64 s[0:1], vcc
	v_add_u32_e32 v3, 0x4000, v2
	v_mov_b32_e32 v1, s3
	ds_write_b64 v1, v[2:3] offset:256
	s_or_b64 exec, exec, s[0:1]

.LBB0_1441:
	s_and_b64 vcc, exec, s[0:1]
	s_cmp_eq_u32 s98, 0
	s_cbranch_scc1 .Lgk_first_p10
	v_mov_b32_e32 v175, v169
	v_mov_b32_e32 v173, v169
	s_mov_b32 s23, 0
	s_mov_b64 s[34:35], 0x100
	s_mov_b64 s[36:37], s[16:17]
	ds_read_b128 v[26:29], v191
	ds_read_b128 v[30:33], v191 offset:1024
	ds_read_b128 v[18:21], v191 offset:2048
	ds_read_b128 v[22:25], v191 offset:3072
	ds_read_b128 v[10:13], v192
	ds_read_b128 v[14:17], v192 offset:1024
	ds_read_b128 v[2:5], v192 offset:2048
	ds_read_b128 v[6:9], v192 offset:3072
	s_cmp_eq_u32 s54, s23
	s_cselect_b64 vcc, -1, 0
	s_add_i32 s23, s23, 2
	s_and_b64 s[38:39], vcc, exec
	s_cselect_b32 s38, 0, s34
	s_cselect_b32 s25, 0, s35
	s_add_u32 s38, s12, s38
	s_addc_u32 s39, s13, s25
	s_add_u32 s25, s30, s34
	s_addc_u32 s67, s31, s35
	s_and_b64 s[40:41], vcc, exec
	v_cndmask_b32_e32 v168, v197, v198, vcc
	v_cndmask_b32_e32 v202, v172, v200, vcc
	v_cndmask_b32_e32 v184, v170, v199, vcc
	s_cselect_b32 s41, s27, s67
	s_cselect_b32 s40, s26, s25
	s_mov_b32 m0, s55
	v_lshl_add_u64 v[186:187], s[36:37], 0, v[172:173]
	ds_read_b128 v[176:179], v193
	ds_read_b128 v[180:183], v193 offset:1024
	ds_read_b128 v[208:211], v193 offset:2048
	ds_read_b128 v[212:215], v193 offset:3072
	ds_read_b128 v[216:219], v193 offset:4096
	ds_read_b128 v[220:223], v193 offset:5120
	ds_read_b128 v[224:227], v193 offset:6144
	ds_read_b128 v[228:231], v193 offset:7168
	global_load_lds_dwordx4 v[186:187], off
	v_lshl_add_u64 v[186:187], s[36:37], 0, v[174:175]
	s_mov_b32 m0, s56
	s_nop 0
	global_load_lds_dwordx4 v[186:187], off
	s_waitcnt vmcnt(16)
	s_waitcnt lgkmcnt(0)
	s_barrier
	s_setprio 1
	s_waitcnt lgkmcnt(0)
	v_mfma_scale_f32_16x16x128_f8f6f4 v[158:161], v[26:33], v[176:183], 0, v188, v189 op_sel_hi:[0,0,0]
	v_mfma_scale_f32_16x16x128_f8f6f4 v[154:157], v[18:25], v[176:183], 0, v188, v189 op_sel_hi:[0,0,0]
	v_mfma_scale_f32_16x16x128_f8f6f4 v[142:145], v[26:33], v[208:215], 0, v188, v189 op_sel_hi:[0,0,0]
	v_mfma_scale_f32_16x16x128_f8f6f4 v[138:141], v[18:25], v[208:215], 0, v188, v189 op_sel_hi:[0,0,0]
	v_mfma_scale_f32_16x16x128_f8f6f4 v[126:129], v[26:33], v[216:223], 0, v188, v189 op_sel_hi:[0,0,0]
	v_mfma_scale_f32_16x16x128_f8f6f4 v[122:125], v[18:25], v[216:223], 0, v188, v189 op_sel_hi:[0,0,0]
	v_mfma_scale_f32_16x16x128_f8f6f4 v[110:113], v[26:33], v[224:231], 0, v188, v189 op_sel_hi:[0,0,0]
	v_mfma_scale_f32_16x16x128_f8f6f4 v[106:109], v[18:25], v[224:231], 0, v188, v189 op_sel_hi:[0,0,0]
	s_setprio 0
	s_setprio 1
	v_mfma_scale_f32_16x16x128_f8f6f4 v[150:153], v[10:17], v[176:183], 0, v188, v189 op_sel_hi:[0,0,0]
	v_mfma_scale_f32_16x16x128_f8f6f4 v[146:149], v[2:9], v[176:183], 0, v188, v189 op_sel_hi:[0,0,0]
	v_mfma_scale_f32_16x16x128_f8f6f4 v[134:137], v[10:17], v[208:215], 0, v188, v189 op_sel_hi:[0,0,0]
	v_mfma_scale_f32_16x16x128_f8f6f4 v[130:133], v[2:9], v[208:215], 0, v188, v189 op_sel_hi:[0,0,0]
	v_mfma_scale_f32_16x16x128_f8f6f4 v[118:121], v[10:17], v[216:223], 0, v188, v189 op_sel_hi:[0,0,0]
	v_mfma_scale_f32_16x16x128_f8f6f4 v[114:117], v[2:9], v[216:223], 0, v188, v189 op_sel_hi:[0,0,0]
	v_mfma_scale_f32_16x16x128_f8f6f4 v[102:105], v[10:17], v[224:231], 0, v188, v189 op_sel_hi:[0,0,0]
	v_mfma_scale_f32_16x16x128_f8f6f4 v[98:101], v[2:9], v[224:231], 0, v188, v189 op_sel_hi:[0,0,0]
	s_setprio 0
	s_barrier
	s_mov_b32 m0, s57
	v_lshl_add_u64 v[176:177], s[40:41], 0, v[166:167]
	v_lshl_add_u64 v[178:179], s[40:41], 0, v[164:165]
	s_add_u32 s40, s40, s10
	ds_read_b128 v[208:211], v193 offset:16384
	ds_read_b128 v[212:215], v193 offset:17408
	ds_read_b128 v[216:219], v193 offset:18432
	ds_read_b128 v[220:223], v193 offset:19456
	ds_read_b128 v[224:227], v193 offset:20480
	ds_read_b128 v[228:231], v193 offset:21504
	ds_read_b128 v[232:235], v193 offset:22528
	ds_read_b128 v[236:239], v193 offset:23552
	global_load_lds_dwordx4 v[176:177], off
	s_mov_b32 m0, s58
	s_addc_u32 s41, s41, s11
	global_load_lds_dwordx4 v[178:179], off
	v_lshl_add_u64 v[180:181], s[40:41], 0, v[166:167]
	s_mov_b32 m0, s59
	v_lshl_add_u64 v[182:183], s[40:41], 0, v[164:165]
	global_load_lds_dwordx4 v[180:181], off
	s_mov_b32 m0, s60
	v_mov_b32_e32 v185, v169
	global_load_lds_dwordx4 v[182:183], off
	s_mov_b32 m0, s29
	v_lshl_add_u64 v[186:187], s[38:39], 0, v[168:169]
	global_load_lds_dwordx4 v168, s[38:39]
	s_mov_b32 m0, s46
	s_nop 0
	global_load_lds_dwordx4 v184, s[38:39]
	s_waitcnt vmcnt(16)
	s_waitcnt lgkmcnt(0)
	v_lshl_add_u64 v[184:185], s[38:39], 0, v[184:185]
	s_barrier
	s_setprio 1
	s_waitcnt lgkmcnt(0)
	v_mfma_scale_f32_16x16x128_f8f6f4 v[94:97], v[26:33], v[208:215], 0, v188, v189 op_sel_hi:[0,0,0]
	v_mfma_scale_f32_16x16x128_f8f6f4 v[90:93], v[18:25], v[208:215], 0, v188, v189 op_sel_hi:[0,0,0]
	v_mfma_scale_f32_16x16x128_f8f6f4 v[78:81], v[26:33], v[216:223], 0, v188, v189 op_sel_hi:[0,0,0]
	v_mfma_scale_f32_16x16x128_f8f6f4 v[74:77], v[18:25], v[216:223], 0, v188, v189 op_sel_hi:[0,0,0]
	v_mfma_scale_f32_16x16x128_f8f6f4 v[62:65], v[26:33], v[224:231], 0, v188, v189 op_sel_hi:[0,0,0]
	v_mfma_scale_f32_16x16x128_f8f6f4 v[58:61], v[18:25], v[224:231], 0, v188, v189 op_sel_hi:[0,0,0]
	v_mfma_scale_f32_16x16x128_f8f6f4 v[46:49], v[26:33], v[232:239], 0, v188, v189 op_sel_hi:[0,0,0]
	v_mfma_scale_f32_16x16x128_f8f6f4 v[42:45], v[18:25], v[232:239], 0, v188, v189 op_sel_hi:[0,0,0]
	s_setprio 0
	s_setprio 1
	v_mfma_scale_f32_16x16x128_f8f6f4 v[86:89], v[10:17], v[208:215], 0, v188, v189 op_sel_hi:[0,0,0]
	v_mfma_scale_f32_16x16x128_f8f6f4 v[82:85], v[2:9], v[208:215], 0, v188, v189 op_sel_hi:[0,0,0]
	v_mfma_scale_f32_16x16x128_f8f6f4 v[70:73], v[10:17], v[216:223], 0, v188, v189 op_sel_hi:[0,0,0]
	v_mfma_scale_f32_16x16x128_f8f6f4 v[66:69], v[2:9], v[216:223], 0, v188, v189 op_sel_hi:[0,0,0]
	v_mfma_scale_f32_16x16x128_f8f6f4 v[54:57], v[10:17], v[224:231], 0, v188, v189 op_sel_hi:[0,0,0]
	v_mfma_scale_f32_16x16x128_f8f6f4 v[50:53], v[2:9], v[224:231], 0, v188, v189 op_sel_hi:[0,0,0]
	v_mfma_scale_f32_16x16x128_f8f6f4 v[38:41], v[10:17], v[232:239], 0, v188, v189 op_sel_hi:[0,0,0]
	v_mfma_scale_f32_16x16x128_f8f6f4 v[34:37], v[2:9], v[232:239], 0, v188, v189 op_sel_hi:[0,0,0]
	s_setprio 0
	s_barrier
	ds_read_b128 v[26:29], v194
	ds_read_b128 v[30:33], v194 offset:1024
	ds_read_b128 v[18:21], v194 offset:2048
	ds_read_b128 v[22:25], v194 offset:3072
	ds_read_b128 v[10:13], v195
	ds_read_b128 v[14:17], v195 offset:1024
	ds_read_b128 v[2:5], v195 offset:2048
	ds_read_b128 v[6:9], v195 offset:3072
	s_mov_b32 m0, s47
	ds_read_b128 v[208:211], v193 offset:32768
	ds_read_b128 v[212:215], v193 offset:33792
	ds_read_b128 v[216:219], v193 offset:34816
	ds_read_b128 v[220:223], v193 offset:35840
	ds_read_b128 v[224:227], v193 offset:36864
	ds_read_b128 v[228:231], v193 offset:37888
	ds_read_b128 v[232:235], v193 offset:38912
	ds_read_b128 v[236:239], v193 offset:39936
	v_cndmask_b32_e32 v168, v174, v201, vcc
	global_load_lds_dwordx4 v202, s[38:39]
	s_mov_b32 m0, s48
	s_nop 0
	global_load_lds_dwordx4 v168, s[38:39]
	s_waitcnt vmcnt(8)
	s_waitcnt lgkmcnt(0)
	s_barrier
	s_setprio 1
	s_waitcnt lgkmcnt(0)
	v_mfma_scale_f32_16x16x128_f8f6f4 v[158:161], v[26:33], v[208:215], v[158:161], v188, v189 op_sel_hi:[0,0,0]
	v_mfma_scale_f32_16x16x128_f8f6f4 v[154:157], v[18:25], v[208:215], v[154:157], v188, v189 op_sel_hi:[0,0,0]
	v_mfma_scale_f32_16x16x128_f8f6f4 v[142:145], v[26:33], v[216:223], v[142:145], v188, v189 op_sel_hi:[0,0,0]
	v_mfma_scale_f32_16x16x128_f8f6f4 v[138:141], v[18:25], v[216:223], v[138:141], v188, v189 op_sel_hi:[0,0,0]
	v_mfma_scale_f32_16x16x128_f8f6f4 v[126:129], v[26:33], v[224:231], v[126:129], v188, v189 op_sel_hi:[0,0,0]
	v_mfma_scale_f32_16x16x128_f8f6f4 v[122:125], v[18:25], v[224:231], v[122:125], v188, v189 op_sel_hi:[0,0,0]
	v_mfma_scale_f32_16x16x128_f8f6f4 v[110:113], v[26:33], v[232:239], v[110:113], v188, v189 op_sel_hi:[0,0,0]
	v_mfma_scale_f32_16x16x128_f8f6f4 v[106:109], v[18:25], v[232:239], v[106:109], v188, v189 op_sel_hi:[0,0,0]
	s_setprio 0
	s_setprio 1
	v_mfma_scale_f32_16x16x128_f8f6f4 v[150:153], v[10:17], v[208:215], v[150:153], v188, v189 op_sel_hi:[0,0,0]
	v_mfma_scale_f32_16x16x128_f8f6f4 v[146:149], v[2:9], v[208:215], v[146:149], v188, v189 op_sel_hi:[0,0,0]
	v_mfma_scale_f32_16x16x128_f8f6f4 v[134:137], v[10:17], v[216:223], v[134:137], v188, v189 op_sel_hi:[0,0,0]
	v_mfma_scale_f32_16x16x128_f8f6f4 v[130:133], v[2:9], v[216:223], v[130:133], v188, v189 op_sel_hi:[0,0,0]
	v_mfma_scale_f32_16x16x128_f8f6f4 v[118:121], v[10:17], v[224:231], v[118:121], v188, v189 op_sel_hi:[0,0,0]
	v_mfma_scale_f32_16x16x128_f8f6f4 v[114:117], v[2:9], v[224:231], v[114:117], v188, v189 op_sel_hi:[0,0,0]
	v_mfma_scale_f32_16x16x128_f8f6f4 v[102:105], v[10:17], v[232:239], v[102:105], v188, v189 op_sel_hi:[0,0,0]
	v_mfma_scale_f32_16x16x128_f8f6f4 v[98:101], v[2:9], v[232:239], v[98:101], v188, v189 op_sel_hi:[0,0,0]
	s_setprio 0
	s_barrier
	s_mov_b32 m0, s61
	v_lshl_add_u64 v[176:177], v[176:177], 0, s[18:19]
	ds_read_b128 v[208:211], v193 offset:49152
	ds_read_b128 v[212:215], v193 offset:50176
	ds_read_b128 v[216:219], v193 offset:51200
	ds_read_b128 v[220:223], v193 offset:52224
	ds_read_b128 v[224:227], v193 offset:53248
	ds_read_b128 v[228:231], v193 offset:54272
	ds_read_b128 v[232:235], v193 offset:55296
	ds_read_b128 v[236:239], v193 offset:56320
	global_load_lds_dwordx4 v[176:177], off
	v_lshl_add_u64 v[176:177], v[178:179], 0, s[18:19]
	s_mov_b32 m0, s62
	s_nop 0
	global_load_lds_dwordx4 v[176:177], off
	v_lshl_add_u64 v[176:177], v[180:181], 0, s[18:19]
	s_mov_b32 m0, s63
	s_nop 0
	global_load_lds_dwordx4 v[176:177], off
	v_lshl_add_u64 v[176:177], v[182:183], 0, s[18:19]
	s_add_i32 m0, s63, 0x2000
	s_nop 0
	global_load_lds_dwordx4 v[176:177], off
	v_lshl_add_u64 v[176:177], v[186:187], 0, s[18:19]
	s_mov_b32 m0, s50
	s_nop 0
	global_load_lds_dwordx4 v[176:177], off
	v_lshl_add_u64 v[176:177], v[184:185], 0, s[18:19]
	s_mov_b32 m0, s51
	s_nop 0
	global_load_lds_dwordx4 v[176:177], off
	s_waitcnt vmcnt(8)
	s_waitcnt lgkmcnt(0)
	s_barrier
	s_setprio 1
	s_waitcnt lgkmcnt(0)
	v_mfma_scale_f32_16x16x128_f8f6f4 v[94:97], v[26:33], v[208:215], v[94:97], v188, v189 op_sel_hi:[0,0,0]
	v_mfma_scale_f32_16x16x128_f8f6f4 v[90:93], v[18:25], v[208:215], v[90:93], v188, v189 op_sel_hi:[0,0,0]
	v_mfma_scale_f32_16x16x128_f8f6f4 v[78:81], v[26:33], v[216:223], v[78:81], v188, v189 op_sel_hi:[0,0,0]
	v_mfma_scale_f32_16x16x128_f8f6f4 v[74:77], v[18:25], v[216:223], v[74:77], v188, v189 op_sel_hi:[0,0,0]
	v_mfma_scale_f32_16x16x128_f8f6f4 v[62:65], v[26:33], v[224:231], v[62:65], v188, v189 op_sel_hi:[0,0,0]
	v_mfma_scale_f32_16x16x128_f8f6f4 v[58:61], v[18:25], v[224:231], v[58:61], v188, v189 op_sel_hi:[0,0,0]
	v_mfma_scale_f32_16x16x128_f8f6f4 v[46:49], v[26:33], v[232:239], v[46:49], v188, v189 op_sel_hi:[0,0,0]
	v_mfma_scale_f32_16x16x128_f8f6f4 v[42:45], v[18:25], v[232:239], v[42:45], v188, v189 op_sel_hi:[0,0,0]
	s_setprio 0
	s_setprio 1
	v_mfma_scale_f32_16x16x128_f8f6f4 v[86:89], v[10:17], v[208:215], v[86:89], v188, v189 op_sel_hi:[0,0,0]
	v_mfma_scale_f32_16x16x128_f8f6f4 v[82:85], v[2:9], v[208:215], v[82:85], v188, v189 op_sel_hi:[0,0,0]
	v_mfma_scale_f32_16x16x128_f8f6f4 v[70:73], v[10:17], v[216:223], v[70:73], v188, v189 op_sel_hi:[0,0,0]
	v_mfma_scale_f32_16x16x128_f8f6f4 v[66:69], v[2:9], v[216:223], v[66:69], v188, v189 op_sel_hi:[0,0,0]
	v_mfma_scale_f32_16x16x128_f8f6f4 v[54:57], v[10:17], v[224:231], v[54:57], v188, v189 op_sel_hi:[0,0,0]
	v_mfma_scale_f32_16x16x128_f8f6f4 v[50:53], v[2:9], v[224:231], v[50:53], v188, v189 op_sel_hi:[0,0,0]
	v_mfma_scale_f32_16x16x128_f8f6f4 v[38:41], v[10:17], v[232:239], v[38:41], v188, v189 op_sel_hi:[0,0,0]
	v_mfma_scale_f32_16x16x128_f8f6f4 v[34:37], v[2:9], v[232:239], v[34:37], v188, v189 op_sel_hi:[0,0,0]
	s_setprio 0
	s_barrier
	s_add_u32 s34, s34, 0x100
	s_addc_u32 s35, s35, 0
	s_add_u32 s36, s36, 0x100
	s_addc_u32 s37, s37, 0
	s_cmp_ge_i32 s23, s49
	s_cbranch_scc1 .LBB0_1444
	s_branch .LBB0_1443

.LBB0_1446:
	v_lshl_or_b32 v10, s28, 8, v190
	v_max_f32_e32 v2, v158, v158
	v_med3_f32 v3, v2, s64, v196
	v_max_f32_e32 v2, v159, v159
	v_med3_f32 v4, v2, s64, v196
	v_mov_b32_e32 v2, v169
	v_cvt_pk_fp8_f32 v2, v3, v4
	v_max_f32_e32 v5, v160, v160
	v_max_f32_e32 v4, v161, v161
	v_med3_f32 v3, v5, s64, v196
	v_med3_f32 v4, v4, s64, v196
	v_cvt_pk_fp8_f32 v2, v3, v4 op_sel:[0,0,1]
	v_max_f32_e32 v3, v154, v154
	v_med3_f32 v4, v3, s64, v196
	v_max_f32_e32 v3, v155, v155
	v_med3_f32 v5, v3, s64, v196
	v_mov_b32_e32 v3, v169
	v_cvt_pk_fp8_f32 v3, v4, v5
	v_max_f32_e32 v6, v156, v156
	v_max_f32_e32 v5, v157, v157
	v_med3_f32 v4, v6, s64, v196
	v_med3_f32 v5, v5, s64, v196
	v_cvt_pk_fp8_f32 v3, v4, v5 op_sel:[0,0,1]
	v_max_f32_e32 v4, v150, v150
	v_med3_f32 v5, v4, s64, v196
	v_max_f32_e32 v4, v151, v151
	v_med3_f32 v6, v4, s64, v196
	v_mov_b32_e32 v4, v169
	v_cvt_pk_fp8_f32 v4, v5, v6
	v_max_f32_e32 v7, v152, v152
	v_max_f32_e32 v6, v153, v153
	v_med3_f32 v5, v7, s64, v196
	v_med3_f32 v6, v6, s64, v196
	v_cvt_pk_fp8_f32 v4, v5, v6 op_sel:[0,0,1]
	v_max_f32_e32 v5, v146, v146
	v_med3_f32 v6, v5, s64, v196
	v_max_f32_e32 v5, v147, v147
	v_med3_f32 v7, v5, s64, v196
	v_mov_b32_e32 v5, v169
	v_cvt_pk_fp8_f32 v5, v6, v7
	v_max_f32_e32 v8, v148, v148
	v_max_f32_e32 v7, v149, v149
	v_med3_f32 v6, v8, s64, v196
	v_med3_f32 v7, v7, s64, v196
	v_cvt_pk_fp8_f32 v5, v6, v7 op_sel:[0,0,1]
	v_max_f32_e32 v6, v142, v142
	v_med3_f32 v7, v6, s64, v196
	v_max_f32_e32 v6, v143, v143
	v_med3_f32 v8, v6, s64, v196
	v_mov_b32_e32 v6, v169
	v_cvt_pk_fp8_f32 v6, v7, v8
	v_max_f32_e32 v9, v144, v144
	v_max_f32_e32 v8, v145, v145
	v_med3_f32 v7, v9, s64, v196
	v_med3_f32 v8, v8, s64, v196
	v_cvt_pk_fp8_f32 v6, v7, v8 op_sel:[0,0,1]
	v_max_f32_e32 v7, v138, v138
	v_med3_f32 v8, v7, s64, v196
	v_max_f32_e32 v7, v139, v139
	v_med3_f32 v9, v7, s64, v196
	v_mov_b32_e32 v7, v169
	v_cvt_pk_fp8_f32 v7, v8, v9
	v_max_f32_e32 v11, v140, v140
	v_max_f32_e32 v9, v141, v141
	v_med3_f32 v8, v11, s64, v196
	v_med3_f32 v9, v9, s64, v196
	v_cvt_pk_fp8_f32 v7, v8, v9 op_sel:[0,0,1]
	v_max_f32_e32 v8, v134, v134
	v_med3_f32 v9, v8, s64, v196
	v_max_f32_e32 v8, v135, v135
	v_med3_f32 v11, v8, s64, v196
	v_mov_b32_e32 v8, v169
	v_cvt_pk_fp8_f32 v8, v9, v11
	v_max_f32_e32 v12, v136, v136
	v_max_f32_e32 v11, v137, v137
	v_med3_f32 v9, v12, s64, v196
	v_med3_f32 v11, v11, s64, v196
	v_cvt_pk_fp8_f32 v8, v9, v11 op_sel:[0,0,1]
	v_max_f32_e32 v9, v130, v130
	v_med3_f32 v11, v9, s64, v196
	v_max_f32_e32 v9, v131, v131
	v_med3_f32 v12, v9, s64, v196
	v_mov_b32_e32 v9, v169
	v_cvt_pk_fp8_f32 v9, v11, v12
	v_max_f32_e32 v13, v132, v132
	v_max_f32_e32 v12, v133, v133
	v_med3_f32 v11, v13, s64, v196
	v_med3_f32 v12, v12, s64, v196
	v_cvt_pk_fp8_f32 v9, v11, v12 op_sel:[0,0,1]
	s_lshl_b32 s23, s66, 19
	v_add3_u32 v10, s23, v171, v10
	buffer_store_dwordx4 v[2:5], v10, s[4:7], 0 offen
	v_max_f32_e32 v11, v108, v108
	v_max_f32_e32 v12, v104, v104
	v_add_u32_e32 v2, 0x8000, v10
	buffer_store_dwordx4 v[6:9], v2, s[4:7], 0 offen
	v_max_f32_e32 v2, v126, v126
	v_med3_f32 v3, v2, s64, v196
	v_max_f32_e32 v2, v127, v127
	v_med3_f32 v4, v2, s64, v196
	v_mov_b32_e32 v2, v169
	v_cvt_pk_fp8_f32 v2, v3, v4
	v_max_f32_e32 v5, v128, v128
	v_max_f32_e32 v4, v129, v129
	v_med3_f32 v3, v5, s64, v196
	v_med3_f32 v4, v4, s64, v196
	v_cvt_pk_fp8_f32 v2, v3, v4 op_sel:[0,0,1]
	v_max_f32_e32 v3, v122, v122
	v_med3_f32 v4, v3, s64, v196
	v_max_f32_e32 v3, v123, v123
	v_med3_f32 v5, v3, s64, v196
	v_mov_b32_e32 v3, v169
	v_cvt_pk_fp8_f32 v3, v4, v5
	v_max_f32_e32 v6, v124, v124
	v_max_f32_e32 v5, v125, v125
	v_med3_f32 v4, v6, s64, v196
	v_med3_f32 v5, v5, s64, v196
	v_cvt_pk_fp8_f32 v3, v4, v5 op_sel:[0,0,1]
	v_max_f32_e32 v4, v118, v118
	v_med3_f32 v5, v4, s64, v196
	v_max_f32_e32 v4, v119, v119
	v_med3_f32 v6, v4, s64, v196
	v_mov_b32_e32 v4, v169
	v_cvt_pk_fp8_f32 v4, v5, v6
	v_max_f32_e32 v7, v120, v120
	v_max_f32_e32 v6, v121, v121
	v_med3_f32 v5, v7, s64, v196
	v_med3_f32 v6, v6, s64, v196
	v_cvt_pk_fp8_f32 v4, v5, v6 op_sel:[0,0,1]
	v_max_f32_e32 v5, v114, v114
	v_med3_f32 v6, v5, s64, v196
	v_max_f32_e32 v5, v115, v115
	v_med3_f32 v7, v5, s64, v196
	v_mov_b32_e32 v5, v169
	v_cvt_pk_fp8_f32 v5, v6, v7
	v_max_f32_e32 v8, v116, v116
	v_max_f32_e32 v7, v117, v117
	v_med3_f32 v6, v8, s64, v196
	v_med3_f32 v7, v7, s64, v196
	v_cvt_pk_fp8_f32 v5, v6, v7 op_sel:[0,0,1]
	v_max_f32_e32 v6, v110, v110
	v_med3_f32 v7, v6, s64, v196
	v_max_f32_e32 v6, v111, v111
	v_med3_f32 v8, v6, s64, v196
	v_mov_b32_e32 v6, v169
	v_cvt_pk_fp8_f32 v6, v7, v8
	v_max_f32_e32 v9, v112, v112
	v_max_f32_e32 v8, v113, v113
	v_med3_f32 v7, v9, s64, v196
	v_med3_f32 v8, v8, s64, v196
	v_cvt_pk_fp8_f32 v6, v7, v8 op_sel:[0,0,1]
	v_max_f32_e32 v7, v106, v106
	v_med3_f32 v8, v7, s64, v196
	v_max_f32_e32 v7, v107, v107
	v_med3_f32 v9, v7, s64, v196
	v_mov_b32_e32 v7, v169
	v_cvt_pk_fp8_f32 v7, v8, v9
	v_max_f32_e32 v9, v109, v109
	v_med3_f32 v8, v11, s64, v196
	v_med3_f32 v9, v9, s64, v196
	v_cvt_pk_fp8_f32 v7, v8, v9 op_sel:[0,0,1]
	v_max_f32_e32 v8, v102, v102
	v_med3_f32 v9, v8, s64, v196
	v_max_f32_e32 v8, v103, v103
	v_med3_f32 v11, v8, s64, v196
	v_mov_b32_e32 v8, v169
	v_cvt_pk_fp8_f32 v8, v9, v11
	v_max_f32_e32 v11, v105, v105
	v_med3_f32 v9, v12, s64, v196
	v_med3_f32 v11, v11, s64, v196
	v_cvt_pk_fp8_f32 v8, v9, v11 op_sel:[0,0,1]
	v_max_f32_e32 v9, v98, v98
	v_med3_f32 v11, v9, s64, v196
	v_max_f32_e32 v9, v99, v99
	v_med3_f32 v12, v9, s64, v196
	v_mov_b32_e32 v9, v169
	v_cvt_pk_fp8_f32 v9, v11, v12
	v_max_f32_e32 v13, v100, v100
	v_max_f32_e32 v12, v101, v101
	v_med3_f32 v11, v13, s64, v196
	v_med3_f32 v12, v12, s64, v196
	v_cvt_pk_fp8_f32 v9, v11, v12 op_sel:[0,0,1]
	v_add_u32_e32 v11, 0x10000, v10
	buffer_store_dwordx4 v[2:5], v11, s[4:7], 0 offen
	v_max_f32_e32 v11, v76, v76
	v_max_f32_e32 v12, v72, v72
	v_add_u32_e32 v2, 0x18000, v10
	buffer_store_dwordx4 v[6:9], v2, s[4:7], 0 offen
	v_max_f32_e32 v2, v94, v94
	v_med3_f32 v3, v2, s64, v196
	v_max_f32_e32 v2, v95, v95
	v_med3_f32 v4, v2, s64, v196
	v_mov_b32_e32 v2, v169
	v_cvt_pk_fp8_f32 v2, v3, v4
	v_max_f32_e32 v5, v96, v96
	v_max_f32_e32 v4, v97, v97
	v_med3_f32 v3, v5, s64, v196
	v_med3_f32 v4, v4, s64, v196
	v_cvt_pk_fp8_f32 v2, v3, v4 op_sel:[0,0,1]
	v_max_f32_e32 v3, v90, v90
	v_med3_f32 v4, v3, s64, v196
	v_max_f32_e32 v3, v91, v91
	v_med3_f32 v5, v3, s64, v196
	v_mov_b32_e32 v3, v169
	v_cvt_pk_fp8_f32 v3, v4, v5
	v_max_f32_e32 v6, v92, v92
	v_max_f32_e32 v5, v93, v93
	v_med3_f32 v4, v6, s64, v196
	v_med3_f32 v5, v5, s64, v196
	v_cvt_pk_fp8_f32 v3, v4, v5 op_sel:[0,0,1]
	v_max_f32_e32 v4, v86, v86
	v_med3_f32 v5, v4, s64, v196
	v_max_f32_e32 v4, v87, v87
	v_med3_f32 v6, v4, s64, v196
	v_mov_b32_e32 v4, v169
	v_cvt_pk_fp8_f32 v4, v5, v6
	v_max_f32_e32 v7, v88, v88
	v_max_f32_e32 v6, v89, v89
	v_med3_f32 v5, v7, s64, v196
	v_med3_f32 v6, v6, s64, v196
	v_cvt_pk_fp8_f32 v4, v5, v6 op_sel:[0,0,1]
	v_max_f32_e32 v5, v82, v82
	v_med3_f32 v6, v5, s64, v196
	v_max_f32_e32 v5, v83, v83
	v_med3_f32 v7, v5, s64, v196
	v_mov_b32_e32 v5, v169
	v_cvt_pk_fp8_f32 v5, v6, v7
	v_max_f32_e32 v8, v84, v84
	v_max_f32_e32 v7, v85, v85
	v_med3_f32 v6, v8, s64, v196
	v_med3_f32 v7, v7, s64, v196
	v_cvt_pk_fp8_f32 v5, v6, v7 op_sel:[0,0,1]
	v_max_f32_e32 v6, v78, v78
	v_med3_f32 v7, v6, s64, v196
	v_max_f32_e32 v6, v79, v79
	v_med3_f32 v8, v6, s64, v196
	v_mov_b32_e32 v6, v169
	v_cvt_pk_fp8_f32 v6, v7, v8
	v_max_f32_e32 v9, v80, v80
	v_max_f32_e32 v8, v81, v81
	v_med3_f32 v7, v9, s64, v196
	v_med3_f32 v8, v8, s64, v196
	v_cvt_pk_fp8_f32 v6, v7, v8 op_sel:[0,0,1]
	v_max_f32_e32 v7, v74, v74
	v_med3_f32 v8, v7, s64, v196
	v_max_f32_e32 v7, v75, v75
	v_med3_f32 v9, v7, s64, v196
	v_mov_b32_e32 v7, v169
	v_cvt_pk_fp8_f32 v7, v8, v9
	v_max_f32_e32 v9, v77, v77
	v_med3_f32 v8, v11, s64, v196
	v_med3_f32 v9, v9, s64, v196
	v_cvt_pk_fp8_f32 v7, v8, v9 op_sel:[0,0,1]
	v_max_f32_e32 v8, v70, v70
	v_med3_f32 v9, v8, s64, v196
	v_max_f32_e32 v8, v71, v71
	v_med3_f32 v11, v8, s64, v196
	v_mov_b32_e32 v8, v169
	v_cvt_pk_fp8_f32 v8, v9, v11
	v_max_f32_e32 v11, v73, v73
	v_med3_f32 v9, v12, s64, v196
	v_med3_f32 v11, v11, s64, v196
	v_cvt_pk_fp8_f32 v8, v9, v11 op_sel:[0,0,1]
	v_max_f32_e32 v9, v66, v66
	v_med3_f32 v11, v9, s64, v196
	v_max_f32_e32 v9, v67, v67
	v_med3_f32 v12, v9, s64, v196
	v_mov_b32_e32 v9, v169
	v_cvt_pk_fp8_f32 v9, v11, v12
	v_max_f32_e32 v13, v68, v68
	v_max_f32_e32 v12, v69, v69
	v_med3_f32 v11, v13, s64, v196
	v_med3_f32 v12, v12, s64, v196
	v_cvt_pk_fp8_f32 v9, v11, v12 op_sel:[0,0,1]
	v_add_u32_e32 v11, 0x40000, v10
	buffer_store_dwordx4 v[2:5], v11, s[4:7], 0 offen
	v_max_f32_e32 v11, v44, v44
	v_max_f32_e32 v12, v40, v40
	v_add_u32_e32 v2, 0x48000, v10
	buffer_store_dwordx4 v[6:9], v2, s[4:7], 0 offen
	v_max_f32_e32 v2, v62, v62
	v_med3_f32 v3, v2, s64, v196
	v_max_f32_e32 v2, v63, v63
	v_med3_f32 v4, v2, s64, v196
	v_mov_b32_e32 v2, v169
	v_cvt_pk_fp8_f32 v2, v3, v4
	v_max_f32_e32 v5, v64, v64
	v_max_f32_e32 v4, v65, v65
	v_med3_f32 v3, v5, s64, v196
	v_med3_f32 v4, v4, s64, v196
	v_cvt_pk_fp8_f32 v2, v3, v4 op_sel:[0,0,1]
	v_max_f32_e32 v3, v58, v58
	v_med3_f32 v4, v3, s64, v196
	v_max_f32_e32 v3, v59, v59
	v_med3_f32 v5, v3, s64, v196
	v_mov_b32_e32 v3, v169
	v_cvt_pk_fp8_f32 v3, v4, v5
	v_max_f32_e32 v6, v60, v60
	v_max_f32_e32 v5, v61, v61
	v_med3_f32 v4, v6, s64, v196
	v_med3_f32 v5, v5, s64, v196
	v_cvt_pk_fp8_f32 v3, v4, v5 op_sel:[0,0,1]
	v_max_f32_e32 v4, v54, v54
	v_med3_f32 v5, v4, s64, v196
	v_max_f32_e32 v4, v55, v55
	v_med3_f32 v6, v4, s64, v196
	v_mov_b32_e32 v4, v169
	v_cvt_pk_fp8_f32 v4, v5, v6
	v_max_f32_e32 v7, v56, v56
	v_max_f32_e32 v6, v57, v57
	v_med3_f32 v5, v7, s64, v196
	v_med3_f32 v6, v6, s64, v196
	v_cvt_pk_fp8_f32 v4, v5, v6 op_sel:[0,0,1]
	v_max_f32_e32 v5, v50, v50
	v_med3_f32 v6, v5, s64, v196
	v_max_f32_e32 v5, v51, v51
	v_med3_f32 v7, v5, s64, v196
	v_mov_b32_e32 v5, v169
	v_cvt_pk_fp8_f32 v5, v6, v7
	v_max_f32_e32 v8, v52, v52
	v_max_f32_e32 v7, v53, v53
	v_med3_f32 v6, v8, s64, v196
	v_med3_f32 v7, v7, s64, v196
	v_cvt_pk_fp8_f32 v5, v6, v7 op_sel:[0,0,1]
	v_max_f32_e32 v6, v46, v46
	v_med3_f32 v7, v6, s64, v196
	v_max_f32_e32 v6, v47, v47
	v_med3_f32 v8, v6, s64, v196
	v_mov_b32_e32 v6, v169
	v_cvt_pk_fp8_f32 v6, v7, v8
	v_max_f32_e32 v9, v48, v48
	v_max_f32_e32 v8, v49, v49
	v_med3_f32 v7, v9, s64, v196
	v_med3_f32 v8, v8, s64, v196
	v_cvt_pk_fp8_f32 v6, v7, v8 op_sel:[0,0,1]
	v_max_f32_e32 v7, v42, v42
	v_med3_f32 v8, v7, s64, v196
	v_max_f32_e32 v7, v43, v43
	v_med3_f32 v9, v7, s64, v196
	v_mov_b32_e32 v7, v169
	v_cvt_pk_fp8_f32 v7, v8, v9
	v_max_f32_e32 v9, v45, v45
	v_med3_f32 v8, v11, s64, v196
	v_med3_f32 v9, v9, s64, v196
	v_cvt_pk_fp8_f32 v7, v8, v9 op_sel:[0,0,1]
	v_max_f32_e32 v8, v38, v38
	v_med3_f32 v9, v8, s64, v196
	v_max_f32_e32 v8, v39, v39
	v_med3_f32 v11, v8, s64, v196
	v_mov_b32_e32 v8, v169
	v_cvt_pk_fp8_f32 v8, v9, v11
	v_max_f32_e32 v11, v41, v41
	v_med3_f32 v9, v12, s64, v196
	v_med3_f32 v11, v11, s64, v196
	v_cvt_pk_fp8_f32 v8, v9, v11 op_sel:[0,0,1]
	v_max_f32_e32 v9, v34, v34
	v_med3_f32 v11, v9, s64, v196
	v_max_f32_e32 v9, v35, v35
	v_med3_f32 v12, v9, s64, v196
	v_mov_b32_e32 v9, v169
	v_cvt_pk_fp8_f32 v9, v11, v12
	v_max_f32_e32 v13, v36, v36
	v_max_f32_e32 v12, v37, v37
	v_med3_f32 v11, v13, s64, v196
	v_med3_f32 v12, v12, s64, v196
	v_cvt_pk_fp8_f32 v9, v11, v12 op_sel:[0,0,1]
	v_add_u32_e32 v11, 0x50000, v10
	buffer_store_dwordx4 v[2:5], v11, s[4:7], 0 offen
	s_and_b64 vcc, exec, s[2:3]
	s_mov_b64 s[2:3], -1
	v_add_u32_e32 v2, 0x58000, v10
	buffer_store_dwordx4 v[6:9], v2, s[4:7], 0 offen
	s_mov_b32 s98, 1
	s_cbranch_vccnz .LBB0_1436
	s_andn2_b64 vcc, exec, s[14:15]
	s_cbranch_vccnz .LBB0_1435
	s_barrier
	s_branch .LBB0_1435
